# v32 + grid barrier: last top-level leader releases all XCD generation words itself (one hop less)
# speedup vs baseline: 1.0024x; 1.0000x over previous
; __device__ __forceinline__ unsigned xb_ld(unsigned* p)              { return __hip_atomic_load(p, __ATOMIC_RELAXED, __HIP_MEMORY_SCOPE_AGENT); }
; __device__ __forceinline__ unsigned xb_add(unsigned* p, unsigned v) { return __hip_atomic_fetch_add(p, v, __ATOMIC_RELAXED, __HIP_MEMORY_SCOPE_AGENT); }
; #define XB_SPIN(cond, bar) do { unsigned _sp = 0; while (cond) { __builtin_amdgcn_s_sleep(1); \
;     if ((++_sp & 255u) == 0u) { if (xb_ld(&(bar)[XB_TMO])) break; if (_sp > XB_SPIN_CAP) { atomicAdd(&(bar)[XB_TMO], 1u); break; } } } } while (0)
; __device__ __forceinline__ void xcd_barrier(const XcdBarrier& b) {
;     ...
;         const unsigned old = xb_add(&bar[XB_XSUB(bx)], 1u);
;         const unsigned gen = old / nloc;
;         if (old + 1u == (gen + 1u) * nloc) {
;             __builtin_amdgcn_fence(__ATOMIC_RELEASE, "agent");
;             asm volatile("s_waitcnt vmcnt(0)" ::: "memory");
;             const unsigned og = xb_add(&bar[XB_TOP], 1u);
;             const unsigned tg = og / nx;
;             if (og + 1u == (tg + 1u) * nx) xb_add(&bar[XB_TOPGEN], 1u);
;             else XB_SPIN(xb_ld(&bar[XB_TOPGEN]) == tg, bar);
;             __builtin_amdgcn_fence(__ATOMIC_ACQUIRE, "agent");
;             xb_add(&bar[XB_XGEN(bx)], 1u);
;             asm volatile("s_waitcnt vmcnt(0)" ::: "memory");
.LBB0_98:
	s_or_b64 exec, exec, s[6:7]
	s_and_saveexec_b64 s[4:5], s[8:9]
	s_cbranch_execz .LBB0_100
	v_mov_b32_e32 v1, 1
	flat_atomic_add v[2:3], v1
	s_add_u32 s6, s38, 0x2400
	s_addc_u32 s7, s39, 0
	v_mov_b64_e32 v[2:3], s[6:7]
	global_atomic_add v[2:3], v1, off
	global_atomic_add v[2:3], v1, off offset:256
	global_atomic_add v[2:3], v1, off offset:512
	global_atomic_add v[2:3], v1, off offset:768
	global_atomic_add v[2:3], v1, off offset:1024
	global_atomic_add v[2:3], v1, off offset:1280
	global_atomic_add v[2:3], v1, off offset:1536
	global_atomic_add v[2:3], v1, off offset:1792
	global_atomic_add v[2:3], v1, off offset:2048
	global_atomic_add v[2:3], v1, off offset:2304
	global_atomic_add v[2:3], v1, off offset:2560
	global_atomic_add v[2:3], v1, off offset:2816
	global_atomic_add v[2:3], v1, off offset:3072
	global_atomic_add v[2:3], v1, off offset:3328
	global_atomic_add v[2:3], v1, off offset:3584
	global_atomic_add v[2:3], v1, off offset:3840
.LBB0_100:
	s_or_b64 exec, exec, s[4:5]
	s_addk_i32 s2, 0x900
	s_mov_b32 s3, 0
	s_lshl_b64 s[2:3], s[2:3], 2
	s_add_u32 s2, s38, s2
	s_addc_u32 s3, s39, s3
	v_mov_b32_e32 v1, 1
	v_mov_b64_e32 v[2:3], s[2:3]
	s_waitcnt vmcnt(0) lgkmcnt(0)
	buffer_inv sc1
	s_waitcnt vmcnt(0)

; __device__ __forceinline__ unsigned xb_ld(unsigned* p)              { return __hip_atomic_load(p, __ATOMIC_RELAXED, __HIP_MEMORY_SCOPE_AGENT); }
; __device__ __forceinline__ unsigned xb_add(unsigned* p, unsigned v) { return __hip_atomic_fetch_add(p, v, __ATOMIC_RELAXED, __HIP_MEMORY_SCOPE_AGENT); }
; #define XB_SPIN(cond, bar) do { unsigned _sp = 0; while (cond) { __builtin_amdgcn_s_sleep(1); \
;     if ((++_sp & 255u) == 0u) { if (xb_ld(&(bar)[XB_TMO])) break; if (_sp > XB_SPIN_CAP) { atomicAdd(&(bar)[XB_TMO], 1u); break; } } } } while (0)
; __device__ __forceinline__ void xcd_barrier(const XcdBarrier& b) {
;     ...
;             __builtin_amdgcn_fence(__ATOMIC_RELEASE, "agent");
;             asm volatile("s_waitcnt vmcnt(0)" ::: "memory");
;             const unsigned og = xb_add(&bar[XB_TOP], 1u);
;             const unsigned tg = og / nx;
;             if (og + 1u == (tg + 1u) * nx) xb_add(&bar[XB_TOPGEN], 1u);
;             else XB_SPIN(xb_ld(&bar[XB_TOPGEN]) == tg, bar);
;             __builtin_amdgcn_fence(__ATOMIC_ACQUIRE, "agent");
;             xb_add(&bar[XB_XGEN(bx)], 1u);
;             asm volatile("s_waitcnt vmcnt(0)" ::: "memory");
.LBB0_102:
	s_or_b64 exec, exec, s[4:5]
	s_add_i32 s66, s2, 0x900
	s_lshl_b64 s[4:5], s[66:67], 2
	s_add_u32 s4, s38, s4
	s_addc_u32 s5, s39, s5
	v_mov_b64_e32 v[2:3], s[4:5]
	s_waitcnt vmcnt(0) lgkmcnt(0)
	buffer_inv sc1
	s_waitcnt vmcnt(0)

; __device__ __forceinline__ unsigned xb_ld(unsigned* p)              { return __hip_atomic_load(p, __ATOMIC_RELAXED, __HIP_MEMORY_SCOPE_AGENT); }
; __device__ __forceinline__ unsigned xb_add(unsigned* p, unsigned v) { return __hip_atomic_fetch_add(p, v, __ATOMIC_RELAXED, __HIP_MEMORY_SCOPE_AGENT); }
; #define XB_SPIN(cond, bar) do { unsigned _sp = 0; while (cond) { __builtin_amdgcn_s_sleep(1); \
;     if ((++_sp & 255u) == 0u) { if (xb_ld(&(bar)[XB_TMO])) break; if (_sp > XB_SPIN_CAP) { atomicAdd(&(bar)[XB_TMO], 1u); break; } } } } while (0)
; __device__ __forceinline__ void xcd_barrier(const XcdBarrier& b) {
;     ...
;         const unsigned old = xb_add(&bar[XB_XSUB(bx)], 1u);
;         const unsigned gen = old / nloc;
;         if (old + 1u == (gen + 1u) * nloc) {
;             __builtin_amdgcn_fence(__ATOMIC_RELEASE, "agent");
;             asm volatile("s_waitcnt vmcnt(0)" ::: "memory");
;             const unsigned og = xb_add(&bar[XB_TOP], 1u);
;             const unsigned tg = og / nx;
;             if (og + 1u == (tg + 1u) * nx) xb_add(&bar[XB_TOPGEN], 1u);
;             else XB_SPIN(xb_ld(&bar[XB_TOPGEN]) == tg, bar);
;             __builtin_amdgcn_fence(__ATOMIC_ACQUIRE, "agent");
;             xb_add(&bar[XB_XGEN(bx)], 1u);
;             asm volatile("s_waitcnt vmcnt(0)" ::: "memory");
.LBB0_197:
	s_or_b64 exec, exec, s[6:7]
	s_and_saveexec_b64 s[4:5], s[8:9]
	s_cbranch_execz .LBB0_199
	flat_atomic_add v[2:3], v238
	s_add_u32 s6, s40, 0x2400
	s_addc_u32 s7, s41, 0
	v_mov_b64_e32 v[2:3], s[6:7]
	global_atomic_add v[2:3], v238, off
	global_atomic_add v[2:3], v238, off offset:256
	global_atomic_add v[2:3], v238, off offset:512
	global_atomic_add v[2:3], v238, off offset:768
	global_atomic_add v[2:3], v238, off offset:1024
	global_atomic_add v[2:3], v238, off offset:1280
	global_atomic_add v[2:3], v238, off offset:1536
	global_atomic_add v[2:3], v238, off offset:1792
	global_atomic_add v[2:3], v238, off offset:2048
	global_atomic_add v[2:3], v238, off offset:2304
	global_atomic_add v[2:3], v238, off offset:2560
	global_atomic_add v[2:3], v238, off offset:2816
	global_atomic_add v[2:3], v238, off offset:3072
	global_atomic_add v[2:3], v238, off offset:3328
	global_atomic_add v[2:3], v238, off offset:3584
	global_atomic_add v[2:3], v238, off offset:3840
.LBB0_199:
	s_or_b64 exec, exec, s[4:5]
	s_add_i32 s66, s2, 0x900
	s_lshl_b64 s[4:5], s[66:67], 2
	s_add_u32 s4, s40, s4
	s_addc_u32 s5, s41, s5
	v_mov_b64_e32 v[2:3], s[4:5]
	s_waitcnt vmcnt(0) lgkmcnt(0)
	buffer_inv sc1
	s_waitcnt vmcnt(0)

; __device__ __forceinline__ unsigned xb_ld(unsigned* p)              { return __hip_atomic_load(p, __ATOMIC_RELAXED, __HIP_MEMORY_SCOPE_AGENT); }
; __device__ __forceinline__ unsigned xb_add(unsigned* p, unsigned v) { return __hip_atomic_fetch_add(p, v, __ATOMIC_RELAXED, __HIP_MEMORY_SCOPE_AGENT); }
; #define XB_SPIN(cond, bar) do { unsigned _sp = 0; while (cond) { __builtin_amdgcn_s_sleep(1); \
;     if ((++_sp & 255u) == 0u) { if (xb_ld(&(bar)[XB_TMO])) break; if (_sp > XB_SPIN_CAP) { atomicAdd(&(bar)[XB_TMO], 1u); break; } } } } while (0)
; __device__ __forceinline__ void xcd_barrier(const XcdBarrier& b) {
;     ...
;             const unsigned og = xb_add(&bar[XB_TOP], 1u);
;             const unsigned tg = og / nx;
;             if (og + 1u == (tg + 1u) * nx) xb_add(&bar[XB_TOPGEN], 1u);
;             else XB_SPIN(xb_ld(&bar[XB_TOPGEN]) == tg, bar);
.LBB0_769:
	s_or_b64 exec, exec, s[6:7]
	s_and_saveexec_b64 s[4:5], s[8:9]
	s_cbranch_execz .LBB0_771
	flat_atomic_add v[2:3], v238
	s_add_u32 s6, s38, 0x2400
	s_addc_u32 s7, s39, 0
	v_mov_b64_e32 v[2:3], s[6:7]
	global_atomic_add v[2:3], v238, off
	global_atomic_add v[2:3], v238, off offset:256
	global_atomic_add v[2:3], v238, off offset:512
	global_atomic_add v[2:3], v238, off offset:768
	global_atomic_add v[2:3], v238, off offset:1024
	global_atomic_add v[2:3], v238, off offset:1280
	global_atomic_add v[2:3], v238, off offset:1536
	global_atomic_add v[2:3], v238, off offset:1792
	global_atomic_add v[2:3], v238, off offset:2048
	global_atomic_add v[2:3], v238, off offset:2304
	global_atomic_add v[2:3], v238, off offset:2560
	global_atomic_add v[2:3], v238, off offset:2816
	global_atomic_add v[2:3], v238, off offset:3072
	global_atomic_add v[2:3], v238, off offset:3328
	global_atomic_add v[2:3], v238, off offset:3584
	global_atomic_add v[2:3], v238, off offset:3840

; __device__ __forceinline__ unsigned xb_ld(unsigned* p)              { return __hip_atomic_load(p, __ATOMIC_RELAXED, __HIP_MEMORY_SCOPE_AGENT); }
; __device__ __forceinline__ unsigned xb_add(unsigned* p, unsigned v) { return __hip_atomic_fetch_add(p, v, __ATOMIC_RELAXED, __HIP_MEMORY_SCOPE_AGENT); }
; #define XB_SPIN(cond, bar) do { unsigned _sp = 0; while (cond) { __builtin_amdgcn_s_sleep(1); \
;     if ((++_sp & 255u) == 0u) { if (xb_ld(&(bar)[XB_TMO])) break; if (_sp > XB_SPIN_CAP) { atomicAdd(&(bar)[XB_TMO], 1u); break; } } } } while (0)
; __device__ __forceinline__ void xcd_barrier(const XcdBarrier& b) {
;     ...
;             const unsigned og = xb_add(&bar[XB_TOP], 1u);
;             const unsigned tg = og / nx;
;             if (og + 1u == (tg + 1u) * nx) xb_add(&bar[XB_TOPGEN], 1u);
;             else XB_SPIN(xb_ld(&bar[XB_TOPGEN]) == tg, bar);
.LBB0_1363:
	flat_atomic_add v[2:3], v238
	s_add_u32 s6, s38, 0x2400
	s_addc_u32 s7, s39, 0
	v_mov_b64_e32 v[2:3], s[6:7]
	global_atomic_add v[2:3], v238, off
	global_atomic_add v[2:3], v238, off offset:256
	global_atomic_add v[2:3], v238, off offset:512
	global_atomic_add v[2:3], v238, off offset:768
	global_atomic_add v[2:3], v238, off offset:1024
	global_atomic_add v[2:3], v238, off offset:1280
	global_atomic_add v[2:3], v238, off offset:1536
	global_atomic_add v[2:3], v238, off offset:1792
	global_atomic_add v[2:3], v238, off offset:2048
	global_atomic_add v[2:3], v238, off offset:2304
	global_atomic_add v[2:3], v238, off offset:2560
	global_atomic_add v[2:3], v238, off offset:2816
	global_atomic_add v[2:3], v238, off offset:3072
	global_atomic_add v[2:3], v238, off offset:3328
	global_atomic_add v[2:3], v238, off offset:3584
	global_atomic_add v[2:3], v238, off offset:3840
	s_getpc_b64 s[98:99]
